# final
# speedup vs baseline: 1.0204x; 1.0204x over previous
amdhsa.kernels:
  - .agpr_count:     0
    .args:
      - .actual_access:  read_only
        .address_space:  global
        .offset:         0
        .size:           8
        .value_kind:     global_buffer
      - .actual_access:  read_only
        .address_space:  global
        .offset:         8
        .size:           8
        .value_kind:     global_buffer
      - .actual_access:  read_only
        .address_space:  global
        .offset:         16
        .size:           8
        .value_kind:     global_buffer
      - .actual_access:  read_only
        .address_space:  global
        .offset:         24
        .size:           8
        .value_kind:     global_buffer
      - .actual_access:  read_only
        .address_space:  global
        .offset:         32
        .size:           8
        .value_kind:     global_buffer
      - .actual_access:  read_only
        .address_space:  global
        .offset:         40
        .size:           8
        .value_kind:     global_buffer
      - .actual_access:  read_only
        .address_space:  global
        .offset:         48
        .size:           8
        .value_kind:     global_buffer
      - .actual_access:  read_only
        .address_space:  global
        .offset:         56
        .size:           8
        .value_kind:     global_buffer
      - .actual_access:  read_only
        .address_space:  global
        .offset:         64
        .size:           8
        .value_kind:     global_buffer
      - .actual_access:  read_only
        .address_space:  global
        .offset:         72
        .size:           8
        .value_kind:     global_buffer
      - .actual_access:  write_only
        .address_space:  global
        .offset:         80
        .size:           8
        .value_kind:     global_buffer
    .group_segment_fixed_size: 13056
    .kernarg_segment_align: 8
    .kernarg_segment_size: 88
    .language:       OpenCL C
    .language_version:
      - 2
      - 0
    .max_flat_workgroup_size: 128
    .name:           _Z11prep_kernelPKfS0_PKiS2_S0_S0_S0_S0_S0_S0_Pc
    .private_segment_fixed_size: 0
    .sgpr_count:     41
    .sgpr_spill_count: 0
    .symbol:         _Z11prep_kernelPKfS0_PKiS2_S0_S0_S0_S0_S0_S0_Pc.kd
    .uniform_work_group_size: 1
    .uses_dynamic_stack: false
    .vgpr_count:     192
    .vgpr_spill_count: 0
    .wavefront_size: 64
  - .agpr_count:     0
    .args:
      - .actual_access:  read_only
        .address_space:  global
        .offset:         0
        .size:           8
        .value_kind:     global_buffer
      - .actual_access:  read_only
        .address_space:  global
        .offset:         8
        .size:           8
        .value_kind:     global_buffer
      - .actual_access:  read_only
        .address_space:  global
        .offset:         16
        .size:           8
        .value_kind:     global_buffer
      - .actual_access:  read_only
        .address_space:  global
        .offset:         24
        .size:           8
        .value_kind:     global_buffer
      - .actual_access:  read_only
        .address_space:  global
        .offset:         32
        .size:           8
        .value_kind:     global_buffer
      - .actual_access:  read_only
        .address_space:  global
        .offset:         40
        .size:           8
        .value_kind:     global_buffer
      - .actual_access:  read_only
        .address_space:  global
        .offset:         48
        .size:           8
        .value_kind:     global_buffer
      - .actual_access:  write_only
        .address_space:  global
        .offset:         56
        .size:           8
        .value_kind:     global_buffer
    .group_segment_fixed_size: 16640
    .kernarg_segment_align: 8
    .kernarg_segment_size: 64
    .language:       OpenCL C
    .language_version:
      - 2
      - 0
    .max_flat_workgroup_size: 256
    .name:           _Z11attn_kernelILi4EEvPKfS1_S1_S1_S1_S1_PKcPf
    .private_segment_fixed_size: 0
    .sgpr_count:     38
    .sgpr_spill_count: 0
    .symbol:         _Z11attn_kernelILi4EEvPKfS1_S1_S1_S1_S1_PKcPf.kd
    .uniform_work_group_size: 1
    .uses_dynamic_stack: false
    .vgpr_count:     256
    .vgpr_spill_count: 0
    .wavefront_size: 64
